# P8 epilogue: exponent scale folded into the clamp affine (one pk_mul fewer per gate pair), bias transforms moved into the first K-loop trip's load interval
# speedup vs baseline: 1.0194x; 1.0194x over previous
; #define PG8_STAGE(bufoff, gbase, voff) do { PG8_GLDS((const char*)(gbase), (voff)[0], ldsb + (bufoff)); PG8_GLDS((const char*)(gbase), (voff)[1], ldsb + (bufoff) + 8192u); } while (0)
; #define PG8_STAGEA(bufoff, gbase, o0, o1) do { PG8_GLDS((const char*)(gbase), (o0), ldsb + (bufoff)); PG8_GLDS((const char*)(gbase), (o1), ldsb + (bufoff) + 8192u); } while (0)
; #define PG8_STAGEA1(bufoff, gbase) do { if constexpr (Sched::GATHER) { PG8_STAGEA(bufoff, gbase, vA2, vA3); } else { PG8_STAGEA(bufoff, (gbase) + hstep, vA0, vA1); } } while (0)
; #define PG8_WAIT_V(n) asm volatile("s_waitcnt vmcnt(" #n ")" ::: "memory")
; #define PG8_BAR __builtin_amdgcn_s_barrier()
; template <class Epi, class Sched, bool F8 = false, bool PF = false, bool I8 = false, int PID = -1>
; __device__ __forceinline__ void gemm_phase(LAS unsigned char* lds, LAS unsigned char* xlds, const int RP, const int RPB, const int nt, const Sched& S, const Epi& E, const int stagger_ticks) {
;     ...
;     PG8_ZERO_ACC();
;     PG8_STAGE(PG8_SB(0, 0), cB, voffB); PG8_STAGE(PG8_SB(0, 1), cB + hstepB, voffB); PG8_STAGEA(PG8_SA(0, 0), cA, vA0, vA1); PG8_STAGEA1(PG8_SA(0, 1), cA);
;     if (wr == 1) PG8_BAR;
;     PG8_WAIT_V(2); PG8_BAR;
;     PG8_STAGE(PG8_SB(1, 0), cB + kstep, voffB); PG8_STAGEA(PG8_SA(1, 0), cA + kstep, vA0, vA1); PG8_STAGE(PG8_SB(1, 1), cB + hstepB + kstep, voffB);
;     PG8_WAIT_V(6); PG8_BAR;
;     static __device__ __forceinline__ f32x2 act2(f32x2 g, f32x2 u) {
;         g.x = __builtin_amdgcn_fmed3f(g.x, -24.0f, 7.0f); g.y = __builtin_amdgcn_fmed3f(g.y, -24.0f, 7.0f);
;         u.x = __builtin_amdgcn_fmed3f(u.x, -7.0f, 7.0f); u.y = __builtin_amdgcn_fmed3f(u.y, -7.0f, 7.0f);
;         f32x2 z = g * (-1.702f * 1.4426950408889634f);
;         f32x2 d; d.x = __builtin_amdgcn_exp2f(z.x); d.y = __builtin_amdgcn_exp2f(z.y);
;         d = d + 1.0f;
;         const float r = __builtin_amdgcn_rcpf(d.x * d.y);
;         f32x2 sg; sg.x = r * d.y; sg.y = r * d.x;
;         return (u + 1.0f) * (g * sg);
.LBB0_954:
	v_and_b32_e32 v2, 48, v6
	v_lshlrev_b32_e32 v3, 6, v6
	s_movk_i32 s15, 0x3c0
	v_and_or_b32 v2, v3, s15, v2
	v_lshlrev_b32_e32 v3, 2, v6
	s_lshl_b32 s44, s2, 6
	s_lshl_b32 s2, s2, 13
	v_and_b32_e32 v3, 32, v3
	v_bitop3_b32 v4, v2, s2, v3 bitop3:0xde
	s_lshl_b32 s2, s3, 5
	s_and_b32 s45, s2, 0x60
	s_lshl_b32 s2, s45, 7
	s_add_u32 s46, s58, 0x2e000000
	s_addc_u32 s47, s59, 0
	v_bitop3_b32 v2, s2, v2, v3 bitop3:0xf6
	s_add_u32 s2, s8, 0x80
	s_addc_u32 s3, s9, 0
	s_add_i32 s15, s42, 0x18000
	s_waitcnt vmcnt(2)
	s_barrier
	s_mov_b32 m0, s15
	s_nop 0
	global_load_lds_dwordx4 v204, s[2:3]
	s_add_i32 s15, s42, 0x1a000
	s_mov_b32 m0, s15
	s_nop 0
	global_load_lds_dwordx4 v205, s[2:3]
	s_add_u32 s2, s6, 0x80
	s_addc_u32 s3, s7, 0
	s_add_i32 s15, s42, 0x8000
	s_mov_b32 m0, s15
	s_nop 0
	global_load_lds_dwordx4 v66, s[2:3]
	s_add_i32 s15, s42, 0xa000
	s_mov_b32 m0, s15
	s_nop 0
	global_load_lds_dwordx4 v67, s[2:3]
	s_add_u32 s2, s8, 0x2080
	s_addc_u32 s3, s9, 0
	s_add_i32 s15, s42, 0x1c000
	s_mov_b32 m0, s15
	s_nop 0
	global_load_lds_dwordx4 v204, s[2:3]
	s_add_i32 s15, s42, 0x1e000
	s_mov_b32 m0, s15
	s_nop 0
	global_load_lds_dwordx4 v205, s[2:3]
	s_waitcnt vmcnt(6)
	s_cmpk_lt_u32 s14, 0x100
	s_cselect_b64 s[14:15], -1, 0
	s_mov_b32 s16, 0x3c800000
	s_mov_b32 s48, 0xc1c00000
	s_mov_b32 s49, 0xc0e00000
	s_mov_b32 s18, 0xc01d265f
	s_mov_b32 s50, 0x20000
	s_mov_b32 s51, 0x24000
	s_mov_b32 s60, 0x28000
	v_add_u32_e32 v206, 0, v2
	v_add_u32_e32 v207, 0, v4
	v_mov_b32_e32 v208, 0x40e00000
	v_mov_b32_e32 v234, 0xc2983d2c
	v_mov_b32_e32 v235, 0x426bb98e
	v_mov_b32_e32 v236, 0xc0b67334
	v_mov_b32_e32 v237, 0x401c62bf
	v_mov_b32_e32 v238, 0x3d042108
	v_mov_b32_e32 v239, 0x3f46318c
	v_mov_b32_e32 v240, 0x3d924925
	v_mov_b32_e32 v241, 0x3f000000
	v_mov_b32_e32 v242, 0x3a042108
	v_mov_b32_e32 v243, 0x3a924925
	s_mov_b64 s[20:21], s[6:7]
	s_barrier
	s_branch .LBB0_957

; #define PG8_STAGE(bufoff, gbase, voff) do { PG8_GLDS((const char*)(gbase), (voff)[0], ldsb + (bufoff)); PG8_GLDS((const char*)(gbase), (voff)[1], ldsb + (bufoff) + 8192u); } while (0)
; #define PG8_STAGEA(bufoff, gbase, o0, o1) do { PG8_GLDS((const char*)(gbase), (o0), ldsb + (bufoff)); PG8_GLDS((const char*)(gbase), (o1), ldsb + (bufoff) + 8192u); } while (0)
; #define PG8_STAGEA1(bufoff, gbase) do { if constexpr (Sched::GATHER) { PG8_STAGEA(bufoff, gbase, vA2, vA3); } else { PG8_STAGEA(bufoff, (gbase) + hstep, vA0, vA1); } } while (0)
; #define PG8_WAIT_VX() do { if (relax) asm volatile("s_waitcnt vmcnt(%0)" :: "n"(8 + Epi::RELAX) : "memory"); else PG8_WAIT_V(8); } while (0)
; template <class Epi, class Sched, bool F8 = false, bool PF = false, bool I8 = false, int PID = -1>
; __device__ __forceinline__ void gemm_phase(LAS unsigned char* lds, LAS unsigned char* xlds, const int RP, const int RPB, const int nt, const Sched& S, const Epi& E, const int stagger_ticks) {
;     ...
;             PG8_LDB(B0, 0, 0); PG8_LDB(B1, 0, 1); PG8_SCHED; PG8_LDA(At, 0, 0); PG8_STAGEA1(PG8_SA(1, 1), a1);
;             if (Sched::GATHER) { if (last) { const u32x4 nv = *nslot; vA0 = nv.x; vA1 = nv.y; vA2 = nv.z; vA3 = nv.w; } }
;             PG8_WAIT_VX(); PG8_WAIT_L(0); PG8_BAR; PG8_MMA(0, 0, At, B0); PG8_MMA(0, 1, At, B1); PG8_BAR; PG8_SCHED;
;             if constexpr (Epi::BIAS_DMA) { if (t == 0 && has_next) E.bias_dma(nxt, xlds + 8192 + ((ui + 1) & 1) * Epi::BIAS_STRIDE, wid, lane); }
;             PG8_LDA(At, 0, 1); PG8_STAGE(PG8_SB(0, 0), b2, voffB); PG8_STAGE(PG8_SB(0, 1), b2 + hstepB, voffB); PG8_STAGEA(PG8_SA(0, 0), a2, vA0, vA1);
;             PG8_WAIT_VX(); PG8_WAIT_L(0); PG8_BAR; PG8_MMA(1, 0, At, B0); PG8_MMA(1, 1, At, B1); PG8_BAR; PG8_SCHED;
;     static __device__ __forceinline__ f32x2 act2(f32x2 g, f32x2 u) {
;         g.x = __builtin_amdgcn_fmed3f(g.x, -24.0f, 7.0f); g.y = __builtin_amdgcn_fmed3f(g.y, -24.0f, 7.0f);
;         u.x = __builtin_amdgcn_fmed3f(u.x, -7.0f, 7.0f); u.y = __builtin_amdgcn_fmed3f(u.y, -7.0f, 7.0f);
;         f32x2 z = g * (-1.702f * 1.4426950408889634f);
;         f32x2 d; d.x = __builtin_amdgcn_exp2f(z.x); d.y = __builtin_amdgcn_exp2f(z.y);
;         d = d + 1.0f;
;         const float r = __builtin_amdgcn_rcpf(d.x * d.y);
;         f32x2 sg; sg.x = r * d.y; sg.y = r * d.x;
;         return (u + 1.0f) * (g * sg);
.Lmy_z958:
	s_add_u32 s28, s2, 0x80
	s_addc_u32 s29, s3, 0
	s_and_b64 s[24:25], s[26:27], exec
	s_cselect_b32 s28, s20, s28
	s_cselect_b32 s29, s21, s29
	s_add_u32 s24, s28, 0x80
	s_addc_u32 s25, s29, 0
	s_waitcnt vmcnt(8)
	s_and_b64 s[26:27], s[26:27], exec
	s_waitcnt lgkmcnt(0)
	s_cselect_b32 s26, s8, s23
	s_cselect_b32 s27, s9, s63
	s_add_u32 s30, s26, 0x80
	s_addc_u32 s31, s27, 0
	s_barrier
	s_setprio 1
	s_waitcnt lgkmcnt(6)
	v_mfma_f32_16x16x128_f8f6f4 v[186:189], v[18:25], v[58:65], 0
	v_mfma_f32_16x16x128_f8f6f4 v[194:197], v[26:33], v[58:65], 0
	s_waitcnt lgkmcnt(4)
	v_mfma_f32_16x16x128_f8f6f4 v[190:193], v[18:25], v[50:57], 0
	v_mfma_f32_16x16x128_f8f6f4 v[182:185], v[26:33], v[50:57], 0
	s_waitcnt lgkmcnt(2)
	v_mfma_f32_16x16x128_f8f6f4 v[154:157], v[18:25], v[42:49], 0
	v_mfma_f32_16x16x128_f8f6f4 v[150:153], v[26:33], v[42:49], 0
	s_waitcnt lgkmcnt(0)
	v_mfma_f32_16x16x128_f8f6f4 v[138:141], v[18:25], v[34:41], 0
	v_mfma_f32_16x16x128_f8f6f4 v[134:137], v[26:33], v[34:41], 0
	v_mfma_f32_16x16x128_f8f6f4 v[174:177], v[2:9], v[58:65], 0
	v_mfma_f32_16x16x128_f8f6f4 v[178:181], v[10:17], v[58:65], 0
	v_mfma_f32_16x16x128_f8f6f4 v[170:173], v[2:9], v[50:57], 0
	v_mfma_f32_16x16x128_f8f6f4 v[166:169], v[10:17], v[50:57], 0
	v_mfma_f32_16x16x128_f8f6f4 v[162:165], v[2:9], v[42:49], 0
	v_mfma_f32_16x16x128_f8f6f4 v[158:161], v[10:17], v[42:49], 0
	v_mfma_f32_16x16x128_f8f6f4 v[146:149], v[2:9], v[34:41], 0
	v_mfma_f32_16x16x128_f8f6f4 v[142:145], v[10:17], v[34:41], 0
	s_setprio 0
	s_barrier
	ds_read_b128 v[34:37], v207 offset:16384
	ds_read_b128 v[38:41], v207 offset:17408
	ds_read_b128 v[42:45], v207 offset:18432
	ds_read_b128 v[46:49], v207 offset:19456
	ds_read_b128 v[50:53], v207 offset:20480
	ds_read_b128 v[54:57], v207 offset:21504
	ds_read_b128 v[58:61], v207 offset:22528
	ds_read_b128 v[62:65], v207 offset:23552
	s_add_i32 s66, s65, 0x10000
	s_mov_b32 m0, s66
	s_nop 0
	global_load_lds_dwordx4 v204, s[26:27]
	s_add_i32 s66, s65, 0x12000
	s_mov_b32 m0, s66
	s_nop 0
	global_load_lds_dwordx4 v205, s[26:27]
	s_add_u32 s66, s26, 0x2000
	s_addc_u32 s67, s27, 0
	s_add_i32 s68, s65, 0x14000
	s_mov_b32 m0, s68
	s_nop 0
	global_load_lds_dwordx4 v204, s[66:67]
	s_add_i32 s68, s65, 0x16000
	s_mov_b32 m0, s68
	s_nop 0
	global_load_lds_dwordx4 v205, s[66:67]
	s_waitcnt vmcnt(6)
	s_waitcnt lgkmcnt(0)
	s_barrier
	s_setprio 1
	s_waitcnt lgkmcnt(6)
	v_mfma_f32_16x16x128_f8f6f4 v[122:125], v[18:25], v[34:41], 0
	v_mfma_f32_16x16x128_f8f6f4 v[118:121], v[26:33], v[34:41], 0
	s_waitcnt lgkmcnt(4)
	v_mfma_f32_16x16x128_f8f6f4 v[106:109], v[18:25], v[42:49], 0
	v_mfma_f32_16x16x128_f8f6f4 v[102:105], v[26:33], v[42:49], 0
	s_mov_b32 m0, s65
	s_nop 0
	global_load_lds_dwordx4 v66, s[28:29]
	s_waitcnt lgkmcnt(2)
	v_mfma_f32_16x16x128_f8f6f4 v[90:93], v[18:25], v[50:57], 0
	v_mfma_f32_16x16x128_f8f6f4 v[86:89], v[26:33], v[50:57], 0
	s_waitcnt lgkmcnt(0)
	v_mfma_f32_16x16x128_f8f6f4 v[74:77], v[18:25], v[58:65], 0
	v_mfma_f32_16x16x128_f8f6f4 v[70:73], v[26:33], v[58:65], 0
	v_mfma_f32_16x16x128_f8f6f4 v[130:133], v[2:9], v[34:41], 0
	v_mfma_f32_16x16x128_f8f6f4 v[126:129], v[10:17], v[34:41], 0
	v_mfma_f32_16x16x128_f8f6f4 v[114:117], v[2:9], v[42:49], 0
	v_mfma_f32_16x16x128_f8f6f4 v[110:113], v[10:17], v[42:49], 0
	s_add_i32 s98, s65, 0x2000
	s_mov_b32 m0, s98
	s_nop 0
	global_load_lds_dwordx4 v67, s[28:29]
	v_mfma_f32_16x16x128_f8f6f4 v[98:101], v[2:9], v[50:57], 0
	v_mfma_f32_16x16x128_f8f6f4 v[94:97], v[10:17], v[50:57], 0
	v_mfma_f32_16x16x128_f8f6f4 v[82:85], v[2:9], v[58:65], 0
	v_mfma_f32_16x16x128_f8f6f4 v[78:81], v[10:17], v[58:65], 0
	s_setprio 0
	s_barrier
	v_pk_fma_f32 v[218:219], v[218:219], v[238:239], v[238:239] op_sel:[0,0,1] op_sel_hi:[1,0,1]
	v_pk_fma_f32 v[220:221], v[220:221], v[238:239], v[238:239] op_sel:[0,0,1] op_sel_hi:[1,0,1]
	v_pk_fma_f32 v[222:223], v[222:223], v[238:239], v[238:239] op_sel:[0,0,1] op_sel_hi:[1,0,1]
	v_pk_fma_f32 v[224:225], v[224:225], v[238:239], v[238:239] op_sel:[0,0,1] op_sel_hi:[1,0,1]
	v_pk_fma_f32 v[214:215], v[214:215], v[240:241], v[240:241] op_sel:[0,0,1] op_sel_hi:[1,0,1]
	v_pk_fma_f32 v[216:217], v[216:217], v[240:241], v[240:241] op_sel:[0,0,1] op_sel_hi:[1,0,1]
	v_pk_fma_f32 v[226:227], v[226:227], v[240:241], v[240:241] op_sel:[0,0,1] op_sel_hi:[1,0,1]
	v_pk_fma_f32 v[228:229], v[228:229], v[240:241], v[240:241] op_sel:[0,0,1] op_sel_hi:[1,0,1]
	v_add_u32_e32 v14, 0x18000, v206
	v_add_u32_e32 v30, 0x1c000, v206
	ds_read_b128 v[2:5], v14
	ds_read_b128 v[6:9], v14 offset:1024
	ds_read_b128 v[10:13], v14 offset:2048
	ds_read_b128 v[14:17], v14 offset:3072
	ds_read_b128 v[18:21], v30
	ds_read_b128 v[22:25], v30 offset:1024
	ds_read_b128 v[26:29], v30 offset:2048
	ds_read_b128 v[30:33], v30 offset:3072
	ds_read_b128 v[34:37], v207 offset:32768
	ds_read_b128 v[38:41], v207 offset:33792
	ds_read_b128 v[42:45], v207 offset:34816
	ds_read_b128 v[46:49], v207 offset:35840
	ds_read_b128 v[50:53], v207 offset:36864
	ds_read_b128 v[54:57], v207 offset:37888
	ds_read_b128 v[58:61], v207 offset:38912
	ds_read_b128 v[62:65], v207 offset:39936
	s_add_i32 s66, s65, 0x4000
	s_mov_b32 m0, s66
	s_nop 0
	global_load_lds_dwordx4 v68, s[28:29]
	s_add_i32 s66, s65, 0x6000
	s_mov_b32 m0, s66
	s_nop 0
	global_load_lds_dwordx4 v69, s[28:29]
	s_waitcnt vmcnt(8)
	s_waitcnt lgkmcnt(0)
	s_barrier
; #define PG8_STAGE(bufoff, gbase, voff) do { PG8_GLDS((const char*)(gbase), (voff)[0], ldsb + (bufoff)); PG8_GLDS((const char*)(gbase), (voff)[1], ldsb + (bufoff) + 8192u); } while (0)
; #define PG8_STAGEA(bufoff, gbase, o0, o1) do { PG8_GLDS((const char*)(gbase), (o0), ldsb + (bufoff)); PG8_GLDS((const char*)(gbase), (o1), ldsb + (bufoff) + 8192u); } while (0)
; #define PG8_STAGEA1(bufoff, gbase) do { if constexpr (Sched::GATHER) { PG8_STAGEA(bufoff, gbase, vA2, vA3); } else { PG8_STAGEA(bufoff, (gbase) + hstep, vA0, vA1); } } while (0)
; #define PG8_LDA(dst, b, h) do { if constexpr (F8) { _Pragma("unroll") for (int m = 0; m < 4; ++m) dst##8[m] = PG8_LD32(lds + PG8_SA(b, h) + aoff + m * 2048); } else { \
;         _Pragma("unroll") for (int m = 0; m < 4; ++m) _Pragma("unroll") for (int k = 0; k < 2; ++k) dst[m][k] = *(const LAS bf16x8*)(lds + PG8_SA(b, h) + aoff + m * 2048 + k * 1024); } } while (0)
; #define PG8_LDB(dst, b, h) do { if constexpr (F8) { _Pragma("unroll") for (int n = 0; n < 2; ++n) dst##8[n] = PG8_LD32(lds + PG8_SB(b, h) + boff + n * 2048); } else { \
;         _Pragma("unroll") for (int n = 0; n < 2; ++n) _Pragma("unroll") for (int k = 0; k < 2; ++k) dst[n][k] = *(const LAS bf16x8*)(lds + PG8_SB(b, h) + boff + n * 2048 + k * 1024); } } while (0)
; #define PG8_WAIT_VR() PG8_WAIT_V(8)
; #define PG8_WAIT_L(n) asm volatile("s_waitcnt lgkmcnt(" #n ")" ::: "memory")
; #define PG8_BAR __builtin_amdgcn_s_barrier()
; #define PG8_SCHED __builtin_amdgcn_sched_barrier(0)
; template <class Epi, class Sched, bool F8 = false, bool PF = false, bool I8 = false, int PID = -1>
; __device__ __forceinline__ void gemm_phase(LAS unsigned char* lds, LAS unsigned char* xlds, const int RP, const int RPB, const int nt, const Sched& S, const Epi& E, const int stagger_ticks) {
;     ...
;             PG8_LDB(B0, 1, 0); PG8_LDB(B1, 1, 1); PG8_SCHED; PG8_LDA(At, 1, 0); PG8_STAGEA1(PG8_SA(0, 1), a2);
;             PG8_WAIT_VR(); PG8_WAIT_L(0); PG8_BAR; PG8_MMA(0, 0, At, B0); PG8_MMA(0, 1, At, B1); PG8_BAR; PG8_SCHED;
;             PG8_LDA(At, 1, 1); PG8_STAGE(PG8_SB(1, 0), b3, voffB); PG8_STAGE(PG8_SB(1, 1), b3 + hstepB, voffB); PG8_STAGEA(PG8_SA(1, 0), a3, vA0, vA1);
;             PG8_WAIT_VR(); PG8_WAIT_L(0); PG8_BAR; PG8_MMA(1, 0, At, B0); PG8_MMA(1, 1, At, B1); PG8_BAR; PG8_SCHED;
	s_setprio 1
	s_waitcnt lgkmcnt(6)
	v_mfma_f32_16x16x128_f8f6f4 v[186:189], v[2:9], v[34:41], v[186:189]
	v_mfma_f32_16x16x128_f8f6f4 v[194:197], v[10:17], v[34:41], v[194:197]
	s_waitcnt lgkmcnt(4)
	v_mfma_f32_16x16x128_f8f6f4 v[190:193], v[2:9], v[42:49], v[190:193]
	v_mfma_f32_16x16x128_f8f6f4 v[182:185], v[10:17], v[42:49], v[182:185]
	s_waitcnt lgkmcnt(2)
	v_mfma_f32_16x16x128_f8f6f4 v[154:157], v[2:9], v[50:57], v[154:157]
	v_mfma_f32_16x16x128_f8f6f4 v[150:153], v[10:17], v[50:57], v[150:153]
	s_waitcnt lgkmcnt(0)
	v_mfma_f32_16x16x128_f8f6f4 v[138:141], v[2:9], v[58:65], v[138:141]
	v_mfma_f32_16x16x128_f8f6f4 v[134:137], v[10:17], v[58:65], v[134:137]
	v_mfma_f32_16x16x128_f8f6f4 v[174:177], v[18:25], v[34:41], v[174:177]
	v_mfma_f32_16x16x128_f8f6f4 v[178:181], v[26:33], v[34:41], v[178:181]
	v_mfma_f32_16x16x128_f8f6f4 v[170:173], v[18:25], v[42:49], v[170:173]
	v_mfma_f32_16x16x128_f8f6f4 v[166:169], v[26:33], v[42:49], v[166:169]
	v_mfma_f32_16x16x128_f8f6f4 v[162:165], v[18:25], v[50:57], v[162:165]
	v_mfma_f32_16x16x128_f8f6f4 v[158:161], v[26:33], v[50:57], v[158:161]
	v_mfma_f32_16x16x128_f8f6f4 v[146:149], v[18:25], v[58:65], v[146:149]
	v_mfma_f32_16x16x128_f8f6f4 v[142:145], v[26:33], v[58:65], v[142:145]
	s_setprio 0
	s_barrier
	ds_read_b128 v[34:37], v207 offset:49152
	ds_read_b128 v[38:41], v207 offset:50176
	ds_read_b128 v[42:45], v207 offset:51200
	ds_read_b128 v[46:49], v207 offset:52224
	ds_read_b128 v[50:53], v207 offset:53248
	ds_read_b128 v[54:57], v207 offset:54272
	ds_read_b128 v[58:61], v207 offset:55296
	ds_read_b128 v[62:65], v207 offset:56320
	s_add_i32 s28, s65, 0x18000
	s_mov_b32 m0, s28
	s_nop 0
	global_load_lds_dwordx4 v204, s[30:31]
	s_add_i32 s28, s65, 0x1a000
	s_mov_b32 m0, s28
	s_nop 0
	global_load_lds_dwordx4 v205, s[30:31]
	s_add_u32 s26, s26, 0x2080
	s_addc_u32 s27, s27, 0
	s_add_i32 s28, s65, 0x1c000
	s_mov_b32 m0, s28
	s_nop 0
	global_load_lds_dwordx4 v204, s[26:27]
	s_add_i32 s28, s65, 0x1e000
	s_mov_b32 m0, s28
	s_nop 0
	global_load_lds_dwordx4 v205, s[26:27]
	s_waitcnt vmcnt(6)
	s_waitcnt lgkmcnt(0)
	s_barrier
	s_setprio 1
	s_waitcnt lgkmcnt(6)
	v_mfma_f32_16x16x128_f8f6f4 v[122:125], v[2:9], v[34:41], v[122:125]
	v_mfma_f32_16x16x128_f8f6f4 v[118:121], v[10:17], v[34:41], v[118:121]
	s_waitcnt lgkmcnt(4)
	v_mfma_f32_16x16x128_f8f6f4 v[106:109], v[2:9], v[42:49], v[106:109]
	v_mfma_f32_16x16x128_f8f6f4 v[102:105], v[10:17], v[42:49], v[102:105]
	s_add_i32 s98, s65, 0x8000
	s_mov_b32 m0, s98
	s_nop 0
	global_load_lds_dwordx4 v66, s[24:25]
	s_waitcnt lgkmcnt(2)
	v_mfma_f32_16x16x128_f8f6f4 v[90:93], v[2:9], v[50:57], v[90:93]
	v_mfma_f32_16x16x128_f8f6f4 v[86:89], v[10:17], v[50:57], v[86:89]
	s_waitcnt lgkmcnt(0)
	v_mfma_f32_16x16x128_f8f6f4 v[74:77], v[2:9], v[58:65], v[74:77]
	v_mfma_f32_16x16x128_f8f6f4 v[70:73], v[10:17], v[58:65], v[70:73]
	v_mfma_f32_16x16x128_f8f6f4 v[130:133], v[18:25], v[34:41], v[130:133]
	v_mfma_f32_16x16x128_f8f6f4 v[126:129], v[26:33], v[34:41], v[126:129]
	v_mfma_f32_16x16x128_f8f6f4 v[114:117], v[18:25], v[42:49], v[114:117]
	v_mfma_f32_16x16x128_f8f6f4 v[110:113], v[26:33], v[42:49], v[110:113]
	s_add_i32 s98, s65, 0xa000
	s_mov_b32 m0, s98
	s_nop 0
	global_load_lds_dwordx4 v67, s[24:25]
	v_mfma_f32_16x16x128_f8f6f4 v[98:101], v[18:25], v[50:57], v[98:101]
	v_mfma_f32_16x16x128_f8f6f4 v[94:97], v[26:33], v[50:57], v[94:97]
	v_mfma_f32_16x16x128_f8f6f4 v[82:85], v[18:25], v[58:65], v[82:85]
	v_mfma_f32_16x16x128_f8f6f4 v[78:81], v[26:33], v[58:65], v[78:81]
	s_setprio 0
	s_barrier
	s_add_i32 s64, s64, 2
	s_add_u32 s23, s23, 0x100
	s_addc_u32 s63, s63, 0
	s_add_u32 s2, s2, 0x100
	s_addc_u32 s3, s3, 0
	s_cmp_gt_u32 s64, 5
	s_branch .LBB0_959

; __device__ __forceinline__ unsigned pk4_fp8(float a, float b, float c, float d) { int w = __builtin_amdgcn_cvt_pk_fp8_f32(a, b, 0, false); w = __builtin_amdgcn_cvt_pk_fp8_f32(c, d, w, true); return (unsigned)w; }
;     static __device__ __forceinline__ f32x2 act2(f32x2 g, f32x2 u) {
;         g.x = __builtin_amdgcn_fmed3f(g.x, -24.0f, 7.0f); g.y = __builtin_amdgcn_fmed3f(g.y, -24.0f, 7.0f);
;         u.x = __builtin_amdgcn_fmed3f(u.x, -7.0f, 7.0f); u.y = __builtin_amdgcn_fmed3f(u.y, -7.0f, 7.0f);
;         f32x2 z = g * (-1.702f * 1.4426950408889634f);
;         f32x2 d; d.x = __builtin_amdgcn_exp2f(z.x); d.y = __builtin_amdgcn_exp2f(z.y);
;         d = d + 1.0f;
;         const float r = __builtin_amdgcn_rcpf(d.x * d.y);
;         f32x2 sg; sg.x = r * d.y; sg.y = r * d.x;
;         return (u + 1.0f) * (g * sg);
;     }
;     __device__ __forceinline__ void operator()(const f32x4 (&acc)[2][2][4][2], const pg8::Unit& u, int wr, int wc, int fr, int fq) const {
;         const int e = u.aux;
;         unsigned char* Ht = ws + WS_H2 + (size_t)u.pm * TSF8;
;         const int hc = u.pn * 128 + wc * 32 + 8 * fq;
;         const f32x4 bg0 = *(const f32x4*)(bgate + e * FF + hc), bg1 = *(const f32x4*)(bgate + e * FF + hc + 4);
;         const f32x4 bu0 = *(const f32x4*)(bup + e * FF + hc), bu1 = *(const f32x4*)(bup + e * FF + hc + 4);
; #pragma unroll
;         for (int ai = 0; ai < 2; ++ai)
; #pragma unroll
;             for (int m = 0; m < 4; ++m) { const int rl = ai * 128 + wr * 64 + m * 16 + fr;
;                 const f32x4 g0 = acc[ai][0][m][0] * (1.0f / 64.0f) + bg0, g1 = acc[ai][0][m][1] * (1.0f / 64.0f) + bg1, u0 = acc[ai][1][m][0] * (1.0f / 64.0f) + bu0, u1 = acc[ai][1][m][1] * (1.0f / 64.0f) + bu1;
;                 const f32x2 h0 = act2((f32x2){g0[0], g0[1]}, (f32x2){u0[0], u0[1]}), h1 = act2((f32x2){g0[2], g0[3]}, (f32x2){u0[2], u0[3]});
;                 const f32x2 h2 = act2((f32x2){g1[0], g1[1]}, (f32x2){u1[0], u1[1]}), h3 = act2((f32x2){g1[2], g1[3]}, (f32x2){u1[2], u1[3]});
;                 *(u32x2*)(Ht + (size_t)rl * FF + hc) = (u32x2){pk4_fp8(h0.x, h0.y, h1.x, h1.y), pk4_fp8(h2.x, h2.y, h3.x, h3.y)}; }
.Lmy_nobar0:
	s_ashr_i32 s23, s22, 31
	s_lshl_b64 s[22:23], s[22:23], 18
	v_mov_b32_e32 v24, v0
	s_add_u32 s22, s46, s22
	s_addc_u32 s23, s47, s23
	s_lshl_b32 s24, s62, 7
	v_lshrrev_b32_e32 v6, 1, v24
	v_and_or_b32 v6, v6, 24, s24
	s_lshl_b32 s24, s61, 10
	s_ashr_i32 s25, s24, 31
	v_or_b32_e32 v22, s45, v6
	s_lshl_b64 s[24:25], s[24:25], 2
	s_add_u32 s26, s84, s24
	v_ashrrev_i32_e32 v23, 31, v22
	s_addc_u32 s27, s85, s25
	v_lshlrev_b64 v[6:7], 2, v[22:23]
	v_lshl_add_u64 v[8:9], s[26:27], 0, v[6:7]
	s_add_u32 s24, s88, s24
	s_addc_u32 s25, s89, s25
	v_lshl_add_u64 v[6:7], s[24:25], 0, v[6:7]
	s_nop 0
	v_and_or_b32 v26, v24, 15, s44
	v_ashrrev_i32_e32 v27, 31, v26
	v_lshlrev_b64 v[32:33], 10, v[26:27]
	v_lshl_add_u64 v[24:25], s[22:23], 0, v[22:23]
	v_lshl_add_u64 v[22:23], v[24:25], 0, v[32:33]
	v_or_b32_e32 v30, 16, v26
	v_pk_fma_f32 v[34:35], v[186:187], v[242:243], v[222:223] op_sel_hi:[1,0,1] clamp
	s_nop 0
	v_pk_fma_f32 v[34:35], v[34:35], v[234:235], v[234:235] op_sel:[0,0,1] op_sel_hi:[1,0,1]
	v_pk_fma_f32 v[32:33], v[188:189], v[242:243], v[224:225] op_sel_hi:[1,0,1] clamp
	v_exp_f32_e32 v56, v34
	v_exp_f32_e32 v57, v35
	v_pk_fma_f32 v[38:39], v[194:195], v[242:243], v[218:219] op_sel_hi:[1,0,1] clamp
	v_pk_fma_f32 v[32:33], v[32:33], v[234:235], v[234:235] op_sel:[0,0,1] op_sel_hi:[1,0,1]
	v_pk_fma_f32 v[38:39], v[38:39], v[234:235], v[234:235] op_sel:[0,0,1] op_sel_hi:[1,0,1]
	v_exp_f32_e32 v58, v32
	v_exp_f32_e32 v59, v33
	v_exp_f32_e32 v60, v38
	v_exp_f32_e32 v61, v39
	v_pk_add_f32 v[56:57], v[56:57], 1.0 op_sel_hi:[1,0]
	v_pk_fma_f32 v[36:37], v[196:197], v[242:243], v[220:221] op_sel_hi:[1,0,1] clamp
	v_mul_f32_e32 v27, v56, v57
	v_pk_fma_f32 v[36:37], v[36:37], v[234:235], v[234:235] op_sel:[0,0,1] op_sel_hi:[1,0,1]
	v_pk_fma_f32 v[64:65], v[172:173], v[242:243], v[228:229] op_sel:[0,1,0] op_sel_hi:[1,1,1] clamp
	v_rcp_f32_e32 v172, v27
	v_pk_add_f32 v[58:59], v[58:59], 1.0 op_sel_hi:[1,0]
	v_exp_f32_e32 v62, v36
	v_exp_f32_e32 v63, v37
	v_pk_add_f32 v[60:61], v[60:61], 1.0 op_sel_hi:[1,0]
	v_pk_fma_f32 v[50:51], v[174:175], v[242:243], v[226:227] op_sel:[0,1,0] op_sel_hi:[1,1,1] clamp
	v_mul_f32_e32 v31, v58, v59
	v_mul_f32_e32 v173, v60, v61
	v_pk_fma_f32 v[50:51], v[50:51], v[236:237], v[236:237] op_sel:[0,0,1] op_sel_hi:[1,0,1]
	v_rcp_f32_e32 v174, v31
	v_pk_mul_f32 v[56:57], v[56:57], v[172:173] op_sel:[1,0] op_sel_hi:[0,0]
	v_pk_mul_f32 v[34:35], v[34:35], v[56:57]
	v_pk_add_f32 v[62:63], v[62:63], 1.0 op_sel_hi:[1,0]
	v_pk_mul_f32 v[34:35], v[50:51], v[34:35]
	v_pk_fma_f32 v[48:49], v[176:177], v[242:243], v[228:229] op_sel:[0,1,0] op_sel_hi:[1,1,1] clamp
	v_mul_f32_e32 v175, v62, v63
	v_cvt_pk_fp8_f32 v28, v34, v35
	v_pk_fma_f32 v[48:49], v[48:49], v[236:237], v[236:237] op_sel:[0,0,1] op_sel_hi:[1,0,1]
	v_pk_mul_f32 v[58:59], v[58:59], v[174:175] op_sel:[1,0] op_sel_hi:[0,0]
	v_pk_fma_f32 v[42:43], v[190:191], v[242:243], v[222:223] op_sel_hi:[1,0,1] clamp
	v_rcp_f32_e32 v176, v173
	v_pk_mul_f32 v[32:33], v[32:33], v[58:59]
	v_pk_fma_f32 v[42:43], v[42:43], v[234:235], v[234:235] op_sel:[0,0,1] op_sel_hi:[1,0,1]
	v_pk_mul_f32 v[32:33], v[48:49], v[32:33]
	v_pk_fma_f32 v[54:55], v[178:179], v[242:243], v[214:215] op_sel:[0,1,0] op_sel_hi:[1,1,1] clamp
	v_cvt_pk_fp8_f32 v28, v32, v33 op_sel:[0,0,1]
	v_rcp_f32_e32 v178, v175
	v_exp_f32_e32 v32, v42
	v_exp_f32_e32 v33, v43
	v_pk_fma_f32 v[54:55], v[54:55], v[236:237], v[236:237] op_sel:[0,0,1] op_sel_hi:[1,0,1]
	v_pk_mul_f32 v[60:61], v[60:61], v[176:177] op_sel:[1,0] op_sel_hi:[0,0]
	v_pk_mul_f32 v[38:39], v[38:39], v[60:61]
	v_pk_fma_f32 v[40:41], v[192:193], v[242:243], v[224:225] op_sel_hi:[1,0,1] clamp
	v_pk_fma_f32 v[52:53], v[180:181], v[242:243], v[216:217] op_sel:[0,1,0] op_sel_hi:[1,1,1] clamp
	v_pk_mul_f32 v[38:39], v[54:55], v[38:39]
	v_pk_fma_f32 v[52:53], v[52:53], v[236:237], v[236:237] op_sel:[0,0,1] op_sel_hi:[1,0,1]
	v_pk_mul_f32 v[62:63], v[62:63], v[178:179] op_sel:[1,0] op_sel_hi:[0,0]
	v_cvt_pk_fp8_f32 v29, v38, v39
	v_pk_add_f32 v[32:33], v[32:33], 1.0 op_sel_hi:[1,0]
	v_pk_fma_f32 v[38:39], v[40:41], v[234:235], v[234:235] op_sel:[0,0,1] op_sel_hi:[1,0,1]
	v_pk_mul_f32 v[36:37], v[36:37], v[62:63]
	v_mul_f32_e32 v27, v32, v33
	v_pk_mul_f32 v[34:35], v[52:53], v[36:37]
	v_rcp_f32_e32 v36, v27
	v_exp_f32_e32 v40, v38
	v_exp_f32_e32 v41, v39
	v_pk_fma_f32 v[46:47], v[182:183], v[242:243], v[218:219] op_sel_hi:[1,0,1] clamp
	v_pk_mul_f32 v[32:33], v[32:33], v[36:37] op_sel:[1,0] op_sel_hi:[0,0]
	v_pk_fma_f32 v[170:171], v[170:171], v[242:243], v[226:227] op_sel:[0,1,0] op_sel_hi:[1,1,1] clamp
	v_pk_add_f32 v[36:37], v[40:41], 1.0 op_sel_hi:[1,0]
	v_cvt_pk_fp8_f32 v29, v34, v35 op_sel:[0,0,1]
	v_mul_f32_e32 v27, v36, v37
	v_rcp_f32_e32 v40, v27
	v_pk_fma_f32 v[34:35], v[170:171], v[236:237], v[236:237] op_sel:[0,0,1] op_sel_hi:[1,0,1]
	v_pk_mul_f32 v[36:37], v[36:37], v[40:41] op_sel:[1,0] op_sel_hi:[0,0]
	v_pk_mul_f32 v[36:37], v[38:39], v[36:37]
	v_pk_fma_f32 v[38:39], v[46:47], v[234:235], v[234:235] op_sel:[0,0,1] op_sel_hi:[1,0,1]
	v_pk_mul_f32 v[32:33], v[42:43], v[32:33]
	v_exp_f32_e32 v40, v38
	v_exp_f32_e32 v41, v39
	v_pk_mul_f32 v[32:33], v[34:35], v[32:33]
	v_pk_fma_f32 v[34:35], v[64:65], v[236:237], v[236:237] op_sel:[0,0,1] op_sel_hi:[1,0,1]
	v_pk_fma_f32 v[44:45], v[184:185], v[242:243], v[220:221] op_sel_hi:[1,0,1] clamp
	v_pk_mul_f32 v[34:35], v[34:35], v[36:37]
	v_pk_add_f32 v[36:37], v[40:41], 1.0 op_sel_hi:[1,0]
	v_pk_fma_f32 v[42:43], v[44:45], v[234:235], v[234:235] op_sel:[0,0,1] op_sel_hi:[1,0,1]
	v_mul_f32_e32 v27, v36, v37
	v_rcp_f32_e32 v40, v27
	global_store_dwordx2 v[22:23], v[28:29], off
	v_exp_f32_e32 v44, v42
; __device__ __forceinline__ unsigned pk4_fp8(float a, float b, float c, float d) { int w = __builtin_amdgcn_cvt_pk_fp8_f32(a, b, 0, false); w = __builtin_amdgcn_cvt_pk_fp8_f32(c, d, w, true); return (unsigned)w; }
;     static __device__ __forceinline__ f32x2 act2(f32x2 g, f32x2 u) {
;         g.x = __builtin_amdgcn_fmed3f(g.x, -24.0f, 7.0f); g.y = __builtin_amdgcn_fmed3f(g.y, -24.0f, 7.0f);
;         u.x = __builtin_amdgcn_fmed3f(u.x, -7.0f, 7.0f); u.y = __builtin_amdgcn_fmed3f(u.y, -7.0f, 7.0f);
;         f32x2 z = g * (-1.702f * 1.4426950408889634f);
;         f32x2 d; d.x = __builtin_amdgcn_exp2f(z.x); d.y = __builtin_amdgcn_exp2f(z.y);
;         d = d + 1.0f;
;         const float r = __builtin_amdgcn_rcpf(d.x * d.y);
;         f32x2 sg; sg.x = r * d.y; sg.y = r * d.x;
;         return (u + 1.0f) * (g * sg);
;     }
;     __device__ __forceinline__ void operator()(const f32x4 (&acc)[2][2][4][2], const pg8::Unit& u, int wr, int wc, int fr, int fq) const {
;         const int e = u.aux;
;         unsigned char* Ht = ws + WS_H2 + (size_t)u.pm * TSF8;
;         const int hc = u.pn * 128 + wc * 32 + 8 * fq;
;         const f32x4 bg0 = *(const f32x4*)(bgate + e * FF + hc), bg1 = *(const f32x4*)(bgate + e * FF + hc + 4);
;         const f32x4 bu0 = *(const f32x4*)(bup + e * FF + hc), bu1 = *(const f32x4*)(bup + e * FF + hc + 4);
; #pragma unroll
;         for (int ai = 0; ai < 2; ++ai)
; #pragma unroll
;             for (int m = 0; m < 4; ++m) { const int rl = ai * 128 + wr * 64 + m * 16 + fr;
;                 const f32x4 g0 = acc[ai][0][m][0] * (1.0f / 64.0f) + bg0, g1 = acc[ai][0][m][1] * (1.0f / 64.0f) + bg1, u0 = acc[ai][1][m][0] * (1.0f / 64.0f) + bu0, u1 = acc[ai][1][m][1] * (1.0f / 64.0f) + bu1;
;                 const f32x2 h0 = act2((f32x2){g0[0], g0[1]}, (f32x2){u0[0], u0[1]}), h1 = act2((f32x2){g0[2], g0[3]}, (f32x2){u0[2], u0[3]});
;                 const f32x2 h2 = act2((f32x2){g1[0], g1[1]}, (f32x2){u1[0], u1[1]}), h3 = act2((f32x2){g1[2], g1[3]}, (f32x2){u1[2], u1[3]});
;                 *(u32x2*)(Ht + (size_t)rl * FF + hc) = (u32x2){pk4_fp8(h0.x, h0.y, h1.x, h1.y), pk4_fp8(h2.x, h2.y, h3.x, h3.y)}; }
	v_exp_f32_e32 v45, v43
	v_pk_mul_f32 v[36:37], v[36:37], v[40:41] op_sel:[1,0] op_sel_hi:[0,0]
	v_pk_mul_f32 v[36:37], v[38:39], v[36:37]
	v_pk_fma_f32 v[28:29], v[166:167], v[242:243], v[214:215] op_sel:[0,1,0] op_sel_hi:[1,1,1] clamp
	v_pk_add_f32 v[38:39], v[44:45], 1.0 op_sel_hi:[1,0]
	v_pk_fma_f32 v[28:29], v[28:29], v[236:237], v[236:237] op_sel:[0,0,1] op_sel_hi:[1,0,1]
	v_mul_f32_e32 v27, v38, v39
	v_rcp_f32_e32 v40, v27
	v_pk_fma_f32 v[168:169], v[168:169], v[242:243], v[216:217] op_sel:[0,1,0] op_sel_hi:[1,1,1] clamp
	v_pk_mul_f32 v[38:39], v[38:39], v[40:41] op_sel:[1,0] op_sel_hi:[0,0]
	v_cvt_pk_fp8_f32 v40, v32, v33
	v_pk_fma_f32 v[32:33], v[154:155], v[242:243], v[222:223] op_sel_hi:[1,0,1] clamp
	v_pk_mul_f32 v[28:29], v[28:29], v[36:37]
	v_pk_fma_f32 v[32:33], v[32:33], v[234:235], v[234:235] op_sel:[0,0,1] op_sel_hi:[1,0,1]
	v_cvt_pk_fp8_f32 v41, v28, v29
	v_exp_f32_e32 v44, v32
	v_exp_f32_e32 v45, v33
	v_pk_fma_f32 v[36:37], v[168:169], v[236:237], v[236:237] op_sel:[0,0,1] op_sel_hi:[1,0,1]
	v_pk_mul_f32 v[28:29], v[42:43], v[38:39]
	v_ashrrev_i32_e32 v31, 31, v30
	v_pk_mul_f32 v[28:29], v[36:37], v[28:29]
	v_pk_add_f32 v[44:45], v[44:45], 1.0 op_sel_hi:[1,0]
	v_cvt_pk_fp8_f32 v41, v28, v29 op_sel:[0,0,1]
	v_lshlrev_b64 v[28:29], 10, v[30:31]
	v_pk_fma_f32 v[30:31], v[156:157], v[242:243], v[224:225] op_sel_hi:[1,0,1] clamp
	v_mul_f32_e32 v27, v44, v45
	v_pk_fma_f32 v[30:31], v[30:31], v[234:235], v[234:235] op_sel:[0,0,1] op_sel_hi:[1,0,1]
	v_rcp_f32_e32 v48, v27
	v_cvt_pk_fp8_f32 v40, v34, v35 op_sel:[0,0,1]
	v_exp_f32_e32 v50, v30
	v_exp_f32_e32 v51, v31
	v_pk_mul_f32 v[44:45], v[44:45], v[48:49] op_sel:[1,0] op_sel_hi:[0,0]
	v_pk_mul_f32 v[32:33], v[32:33], v[44:45]
	v_lshl_add_u64 v[28:29], v[24:25], 0, v[28:29]
	v_pk_add_f32 v[44:45], v[50:51], 1.0 op_sel_hi:[1,0]
	global_store_dwordx2 v[28:29], v[40:41], off
	v_mul_f32_e32 v27, v44, v45
	v_rcp_f32_e32 v48, v27
	v_pk_fma_f32 v[40:41], v[162:163], v[242:243], v[226:227] op_sel:[0,1,0] op_sel_hi:[1,1,1] clamp
	v_pk_fma_f32 v[36:37], v[150:151], v[242:243], v[218:219] op_sel_hi:[1,0,1] clamp
	v_pk_fma_f32 v[40:41], v[40:41], v[236:237], v[236:237] op_sel:[0,0,1] op_sel_hi:[1,0,1]
	v_pk_fma_f32 v[36:37], v[36:37], v[234:235], v[234:235] op_sel:[0,0,1] op_sel_hi:[1,0,1]
	v_pk_mul_f32 v[32:33], v[40:41], v[32:33]
	v_pk_mul_f32 v[40:41], v[44:45], v[48:49] op_sel:[1,0] op_sel_hi:[0,0]
	v_pk_mul_f32 v[30:31], v[30:31], v[40:41]
	v_pk_fma_f32 v[38:39], v[164:165], v[242:243], v[228:229] op_sel:[0,1,0] op_sel_hi:[1,1,1] clamp
	v_exp_f32_e32 v40, v36
	v_exp_f32_e32 v41, v37
	v_pk_fma_f32 v[34:35], v[152:153], v[242:243], v[220:221] op_sel_hi:[1,0,1] clamp
	v_pk_fma_f32 v[38:39], v[38:39], v[236:237], v[236:237] op_sel:[0,0,1] op_sel_hi:[1,0,1]
	v_pk_add_f32 v[40:41], v[40:41], 1.0 op_sel_hi:[1,0]
	v_pk_fma_f32 v[46:47], v[158:159], v[242:243], v[214:215] op_sel:[0,1,0] op_sel_hi:[1,1,1] clamp
	v_mul_f32_e32 v27, v40, v41
	v_pk_fma_f32 v[34:35], v[34:35], v[234:235], v[234:235] op_sel:[0,0,1] op_sel_hi:[1,0,1]
	v_pk_mul_f32 v[30:31], v[38:39], v[30:31]
	v_pk_fma_f32 v[38:39], v[46:47], v[236:237], v[236:237] op_sel:[0,0,1] op_sel_hi:[1,0,1]
	v_rcp_f32_e32 v44, v27
	v_pk_fma_f32 v[42:43], v[160:161], v[242:243], v[216:217] op_sel:[0,1,0] op_sel_hi:[1,1,1] clamp
	v_exp_f32_e32 v46, v34
	v_exp_f32_e32 v47, v35
	v_pk_mul_f32 v[40:41], v[40:41], v[44:45] op_sel:[1,0] op_sel_hi:[0,0]
	v_pk_mul_f32 v[36:37], v[36:37], v[40:41]
	v_pk_add_f32 v[40:41], v[46:47], 1.0 op_sel_hi:[1,0]
	v_pk_mul_f32 v[36:37], v[38:39], v[36:37]
	v_mul_f32_e32 v27, v40, v41
	v_rcp_f32_e32 v44, v27
	v_pk_fma_f32 v[38:39], v[42:43], v[236:237], v[236:237] op_sel:[0,0,1] op_sel_hi:[1,0,1]
	v_cvt_pk_fp8_f32 v42, v32, v33
	v_cvt_pk_fp8_f32 v43, v36, v37
	v_pk_mul_f32 v[40:41], v[40:41], v[44:45] op_sel:[1,0] op_sel_hi:[0,0]
	v_pk_mul_f32 v[32:33], v[34:35], v[40:41]
	v_or_b32_e32 v28, 32, v26
	v_pk_mul_f32 v[32:33], v[38:39], v[32:33]
	v_cvt_pk_fp8_f32 v42, v30, v31 op_sel:[0,0,1]
	v_cvt_pk_fp8_f32 v43, v32, v33 op_sel:[0,0,1]
	v_ashrrev_i32_e32 v29, 31, v28
	v_lshlrev_b64 v[28:29], 10, v[28:29]
	v_pk_fma_f32 v[30:31], v[138:139], v[242:243], v[222:223] op_sel_hi:[1,0,1] clamp
	v_lshl_add_u64 v[28:29], v[24:25], 0, v[28:29]
	v_pk_fma_f32 v[30:31], v[30:31], v[234:235], v[234:235] op_sel:[0,0,1] op_sel_hi:[1,0,1]
	global_store_dwordx2 v[28:29], v[42:43], off
	v_pk_fma_f32 v[28:29], v[140:141], v[242:243], v[224:225] op_sel_hi:[1,0,1] clamp
	v_exp_f32_e32 v42, v30
	v_exp_f32_e32 v43, v31
	v_pk_fma_f32 v[28:29], v[28:29], v[234:235], v[234:235] op_sel:[0,0,1] op_sel_hi:[1,0,1]
	v_pk_add_f32 v[42:43], v[42:43], 1.0 op_sel_hi:[1,0]
	v_exp_f32_e32 v48, v28
	v_mul_f32_e32 v27, v42, v43
	v_rcp_f32_e32 v46, v27
	v_exp_f32_e32 v49, v29
	v_pk_fma_f32 v[38:39], v[146:147], v[242:243], v[226:227] op_sel:[0,1,0] op_sel_hi:[1,1,1] clamp
	v_pk_fma_f32 v[34:35], v[134:135], v[242:243], v[218:219] op_sel_hi:[1,0,1] clamp
	v_pk_mul_f32 v[42:43], v[42:43], v[46:47] op_sel:[1,0] op_sel_hi:[0,0]
	v_pk_mul_f32 v[30:31], v[30:31], v[42:43]
	v_pk_add_f32 v[42:43], v[48:49], 1.0 op_sel_hi:[1,0]
	v_pk_fma_f32 v[38:39], v[38:39], v[236:237], v[236:237] op_sel:[0,0,1] op_sel_hi:[1,0,1]
	v_mul_f32_e32 v27, v42, v43
	v_rcp_f32_e32 v46, v27
	v_pk_fma_f32 v[34:35], v[34:35], v[234:235], v[234:235] op_sel:[0,0,1] op_sel_hi:[1,0,1]
	v_pk_mul_f32 v[30:31], v[38:39], v[30:31]
	v_pk_mul_f32 v[38:39], v[42:43], v[46:47] op_sel:[1,0] op_sel_hi:[0,0]
	v_pk_mul_f32 v[28:29], v[28:29], v[38:39]
	v_pk_fma_f32 v[36:37], v[148:149], v[242:243], v[228:229] op_sel:[0,1,0] op_sel_hi:[1,1,1] clamp
	v_exp_f32_e32 v38, v34
	v_exp_f32_e32 v39, v35
; __device__ __forceinline__ unsigned pk4_fp8(float a, float b, float c, float d) { int w = __builtin_amdgcn_cvt_pk_fp8_f32(a, b, 0, false); w = __builtin_amdgcn_cvt_pk_fp8_f32(c, d, w, true); return (unsigned)w; }
;     static __device__ __forceinline__ f32x2 act2(f32x2 g, f32x2 u) {
;         g.x = __builtin_amdgcn_fmed3f(g.x, -24.0f, 7.0f); g.y = __builtin_amdgcn_fmed3f(g.y, -24.0f, 7.0f);
;         u.x = __builtin_amdgcn_fmed3f(u.x, -7.0f, 7.0f); u.y = __builtin_amdgcn_fmed3f(u.y, -7.0f, 7.0f);
;         f32x2 z = g * (-1.702f * 1.4426950408889634f);
;         f32x2 d; d.x = __builtin_amdgcn_exp2f(z.x); d.y = __builtin_amdgcn_exp2f(z.y);
;         d = d + 1.0f;
;         const float r = __builtin_amdgcn_rcpf(d.x * d.y);
;         f32x2 sg; sg.x = r * d.y; sg.y = r * d.x;
;         return (u + 1.0f) * (g * sg);
;     }
;     __device__ __forceinline__ void operator()(const f32x4 (&acc)[2][2][4][2], const pg8::Unit& u, int wr, int wc, int fr, int fq) const {
;         const int e = u.aux;
;         unsigned char* Ht = ws + WS_H2 + (size_t)u.pm * TSF8;
;         const int hc = u.pn * 128 + wc * 32 + 8 * fq;
;         const f32x4 bg0 = *(const f32x4*)(bgate + e * FF + hc), bg1 = *(const f32x4*)(bgate + e * FF + hc + 4);
;         const f32x4 bu0 = *(const f32x4*)(bup + e * FF + hc), bu1 = *(const f32x4*)(bup + e * FF + hc + 4);
; #pragma unroll
;         for (int ai = 0; ai < 2; ++ai)
; #pragma unroll
;             for (int m = 0; m < 4; ++m) { const int rl = ai * 128 + wr * 64 + m * 16 + fr;
;                 const f32x4 g0 = acc[ai][0][m][0] * (1.0f / 64.0f) + bg0, g1 = acc[ai][0][m][1] * (1.0f / 64.0f) + bg1, u0 = acc[ai][1][m][0] * (1.0f / 64.0f) + bu0, u1 = acc[ai][1][m][1] * (1.0f / 64.0f) + bu1;
;                 const f32x2 h0 = act2((f32x2){g0[0], g0[1]}, (f32x2){u0[0], u0[1]}), h1 = act2((f32x2){g0[2], g0[3]}, (f32x2){u0[2], u0[3]});
;                 const f32x2 h2 = act2((f32x2){g1[0], g1[1]}, (f32x2){u1[0], u1[1]}), h3 = act2((f32x2){g1[2], g1[3]}, (f32x2){u1[2], u1[3]});
;                 *(u32x2*)(Ht + (size_t)rl * FF + hc) = (u32x2){pk4_fp8(h0.x, h0.y, h1.x, h1.y), pk4_fp8(h2.x, h2.y, h3.x, h3.y)}; }
	v_pk_fma_f32 v[32:33], v[136:137], v[242:243], v[220:221] op_sel_hi:[1,0,1] clamp
	v_pk_fma_f32 v[36:37], v[36:37], v[236:237], v[236:237] op_sel:[0,0,1] op_sel_hi:[1,0,1]
	v_pk_add_f32 v[38:39], v[38:39], 1.0 op_sel_hi:[1,0]
	v_pk_fma_f32 v[44:45], v[142:143], v[242:243], v[214:215] op_sel:[0,1,0] op_sel_hi:[1,1,1] clamp
	v_mul_f32_e32 v27, v38, v39
	v_pk_fma_f32 v[32:33], v[32:33], v[234:235], v[234:235] op_sel:[0,0,1] op_sel_hi:[1,0,1]
	v_pk_mul_f32 v[28:29], v[36:37], v[28:29]
	v_pk_fma_f32 v[36:37], v[44:45], v[236:237], v[236:237] op_sel:[0,0,1] op_sel_hi:[1,0,1]
	v_rcp_f32_e32 v42, v27
	v_or_b32_e32 v26, 48, v26
	v_exp_f32_e32 v44, v32
	v_exp_f32_e32 v45, v33
	v_pk_mul_f32 v[38:39], v[38:39], v[42:43] op_sel:[1,0] op_sel_hi:[0,0]
	v_pk_mul_f32 v[34:35], v[34:35], v[38:39]
	v_pk_fma_f32 v[40:41], v[144:145], v[242:243], v[216:217] op_sel:[0,1,0] op_sel_hi:[1,1,1] clamp
	v_pk_add_f32 v[38:39], v[44:45], 1.0 op_sel_hi:[1,0]
	v_mul_f32_e32 v27, v38, v39
	v_rcp_f32_e32 v42, v27
	v_pk_mul_f32 v[34:35], v[36:37], v[34:35]
	v_pk_fma_f32 v[36:37], v[40:41], v[236:237], v[236:237] op_sel:[0,0,1] op_sel_hi:[1,0,1]
	v_ashrrev_i32_e32 v27, 31, v26
	v_cvt_pk_fp8_f32 v40, v30, v31
	v_cvt_pk_fp8_f32 v41, v34, v35
	v_lshlrev_b64 v[26:27], 10, v[26:27]
	v_pk_mul_f32 v[38:39], v[38:39], v[42:43] op_sel:[1,0] op_sel_hi:[0,0]
	v_lshl_add_u64 v[24:25], v[24:25], 0, v[26:27]
	v_pk_fma_f32 v[26:27], v[122:123], v[242:243], v[222:223] op_sel_hi:[1,0,1] clamp
	v_pk_mul_f32 v[30:31], v[32:33], v[38:39]
	v_pk_fma_f32 v[26:27], v[26:27], v[234:235], v[234:235] op_sel:[0,0,1] op_sel_hi:[1,0,1]
	v_pk_mul_f32 v[30:31], v[36:37], v[30:31]
	v_cvt_pk_fp8_f32 v40, v28, v29 op_sel:[0,0,1]
	v_cvt_pk_fp8_f32 v41, v30, v31 op_sel:[0,0,1]
	v_exp_f32_e32 v38, v26
	v_exp_f32_e32 v39, v27
	v_pk_fma_f32 v[34:35], v[130:131], v[242:243], v[226:227] op_sel:[0,1,0] op_sel_hi:[1,1,1] clamp
	global_store_dwordx2 v[24:25], v[40:41], off
	v_pk_fma_f32 v[24:25], v[124:125], v[242:243], v[224:225] op_sel_hi:[1,0,1] clamp
	v_pk_add_f32 v[38:39], v[38:39], 1.0 op_sel_hi:[1,0]
	v_pk_fma_f32 v[24:25], v[24:25], v[234:235], v[234:235] op_sel:[0,0,1] op_sel_hi:[1,0,1]
	v_mul_f32_e32 v42, v38, v39
	v_rcp_f32_e32 v42, v42
	v_pk_fma_f32 v[34:35], v[34:35], v[236:237], v[236:237] op_sel:[0,0,1] op_sel_hi:[1,0,1]
	v_exp_f32_e32 v44, v24
	v_exp_f32_e32 v45, v25
	v_pk_mul_f32 v[38:39], v[38:39], v[42:43] op_sel:[1,0] op_sel_hi:[0,0]
	v_pk_mul_f32 v[26:27], v[26:27], v[38:39]
	v_pk_add_f32 v[38:39], v[44:45], 1.0 op_sel_hi:[1,0]
	v_pk_fma_f32 v[30:31], v[118:119], v[242:243], v[218:219] op_sel_hi:[1,0,1] clamp
	v_mul_f32_e32 v42, v38, v39
	v_rcp_f32_e32 v42, v42
	v_pk_fma_f32 v[30:31], v[30:31], v[234:235], v[234:235] op_sel:[0,0,1] op_sel_hi:[1,0,1]
	v_pk_mul_f32 v[26:27], v[34:35], v[26:27]
	v_pk_mul_f32 v[34:35], v[38:39], v[42:43] op_sel:[1,0] op_sel_hi:[0,0]
	v_pk_mul_f32 v[24:25], v[24:25], v[34:35]
	v_pk_fma_f32 v[32:33], v[132:133], v[242:243], v[228:229] op_sel:[0,1,0] op_sel_hi:[1,1,1] clamp
	v_exp_f32_e32 v34, v30
	v_exp_f32_e32 v35, v31
	v_pk_fma_f32 v[28:29], v[120:121], v[242:243], v[220:221] op_sel_hi:[1,0,1] clamp
	v_pk_fma_f32 v[32:33], v[32:33], v[236:237], v[236:237] op_sel:[0,0,1] op_sel_hi:[1,0,1]
	v_pk_add_f32 v[34:35], v[34:35], 1.0 op_sel_hi:[1,0]
	v_pk_fma_f32 v[40:41], v[126:127], v[242:243], v[214:215] op_sel:[0,1,0] op_sel_hi:[1,1,1] clamp
	v_mul_f32_e32 v38, v34, v35
	v_pk_fma_f32 v[28:29], v[28:29], v[234:235], v[234:235] op_sel:[0,0,1] op_sel_hi:[1,0,1]
	v_pk_mul_f32 v[24:25], v[32:33], v[24:25]
	v_pk_fma_f32 v[32:33], v[40:41], v[236:237], v[236:237] op_sel:[0,0,1] op_sel_hi:[1,0,1]
	v_rcp_f32_e32 v38, v38
	v_pk_fma_f32 v[36:37], v[128:129], v[242:243], v[216:217] op_sel:[0,1,0] op_sel_hi:[1,1,1] clamp
	v_exp_f32_e32 v40, v28
	v_exp_f32_e32 v41, v29
	v_pk_mul_f32 v[34:35], v[34:35], v[38:39] op_sel:[1,0] op_sel_hi:[0,0]
	v_pk_mul_f32 v[30:31], v[30:31], v[34:35]
	v_pk_add_f32 v[34:35], v[40:41], 1.0 op_sel_hi:[1,0]
	v_pk_mul_f32 v[30:31], v[32:33], v[30:31]
	v_mul_f32_e32 v38, v34, v35
	v_rcp_f32_e32 v38, v38
	v_pk_fma_f32 v[32:33], v[36:37], v[236:237], v[236:237] op_sel:[0,0,1] op_sel_hi:[1,0,1]
	v_cvt_pk_fp8_f32 v37, v30, v31
	v_pk_mul_f32 v[34:35], v[34:35], v[38:39] op_sel:[1,0] op_sel_hi:[0,0]
	v_cvt_pk_fp8_f32 v36, v26, v27
	v_pk_mul_f32 v[26:27], v[28:29], v[34:35]
	v_pk_fma_f32 v[34:35], v[114:115], v[242:243], v[226:227] op_sel:[0,1,0] op_sel_hi:[1,1,1] clamp
	v_pk_mul_f32 v[26:27], v[32:33], v[26:27]
	v_cvt_pk_fp8_f32 v36, v24, v25 op_sel:[0,0,1]
	v_cvt_pk_fp8_f32 v37, v26, v27 op_sel:[0,0,1]
	v_pk_fma_f32 v[26:27], v[106:107], v[242:243], v[222:223] op_sel_hi:[1,0,1] clamp
	v_add_co_u32_e32 v24, vcc, s50, v22
	v_pk_fma_f32 v[26:27], v[26:27], v[234:235], v[234:235] op_sel:[0,0,1] op_sel_hi:[1,0,1]
	v_addc_co_u32_e32 v25, vcc, 0, v23, vcc
	v_exp_f32_e32 v38, v26
	v_exp_f32_e32 v39, v27
	global_store_dwordx2 v[24:25], v[36:37], off
	v_pk_fma_f32 v[24:25], v[108:109], v[242:243], v[224:225] op_sel_hi:[1,0,1] clamp
	v_pk_fma_f32 v[34:35], v[34:35], v[236:237], v[236:237] op_sel:[0,0,1] op_sel_hi:[1,0,1]
	v_pk_add_f32 v[38:39], v[38:39], 1.0 op_sel_hi:[1,0]
	v_pk_fma_f32 v[24:25], v[24:25], v[234:235], v[234:235] op_sel:[0,0,1] op_sel_hi:[1,0,1]
	v_mul_f32_e32 v42, v38, v39
	v_rcp_f32_e32 v42, v42
	v_exp_f32_e32 v44, v24
	v_exp_f32_e32 v45, v25
	v_pk_mul_f32 v[38:39], v[38:39], v[42:43] op_sel:[1,0] op_sel_hi:[0,0]
	v_pk_mul_f32 v[26:27], v[26:27], v[38:39]
	v_pk_fma_f32 v[30:31], v[102:103], v[242:243], v[218:219] op_sel_hi:[1,0,1] clamp
	v_pk_add_f32 v[38:39], v[44:45], 1.0 op_sel_hi:[1,0]
	v_mul_f32_e32 v42, v38, v39
	v_rcp_f32_e32 v42, v42
; __device__ __forceinline__ unsigned pk4_fp8(float a, float b, float c, float d) { int w = __builtin_amdgcn_cvt_pk_fp8_f32(a, b, 0, false); w = __builtin_amdgcn_cvt_pk_fp8_f32(c, d, w, true); return (unsigned)w; }
;     static __device__ __forceinline__ f32x2 act2(f32x2 g, f32x2 u) {
;         g.x = __builtin_amdgcn_fmed3f(g.x, -24.0f, 7.0f); g.y = __builtin_amdgcn_fmed3f(g.y, -24.0f, 7.0f);
;         u.x = __builtin_amdgcn_fmed3f(u.x, -7.0f, 7.0f); u.y = __builtin_amdgcn_fmed3f(u.y, -7.0f, 7.0f);
;         f32x2 z = g * (-1.702f * 1.4426950408889634f);
;         f32x2 d; d.x = __builtin_amdgcn_exp2f(z.x); d.y = __builtin_amdgcn_exp2f(z.y);
;         d = d + 1.0f;
;         const float r = __builtin_amdgcn_rcpf(d.x * d.y);
;         f32x2 sg; sg.x = r * d.y; sg.y = r * d.x;
;         return (u + 1.0f) * (g * sg);
;     }
;     __device__ __forceinline__ void operator()(const f32x4 (&acc)[2][2][4][2], const pg8::Unit& u, int wr, int wc, int fr, int fq) const {
;         const int e = u.aux;
;         unsigned char* Ht = ws + WS_H2 + (size_t)u.pm * TSF8;
;         const int hc = u.pn * 128 + wc * 32 + 8 * fq;
;         const f32x4 bg0 = *(const f32x4*)(bgate + e * FF + hc), bg1 = *(const f32x4*)(bgate + e * FF + hc + 4);
;         const f32x4 bu0 = *(const f32x4*)(bup + e * FF + hc), bu1 = *(const f32x4*)(bup + e * FF + hc + 4);
; #pragma unroll
;         for (int ai = 0; ai < 2; ++ai)
; #pragma unroll
;             for (int m = 0; m < 4; ++m) { const int rl = ai * 128 + wr * 64 + m * 16 + fr;
;                 const f32x4 g0 = acc[ai][0][m][0] * (1.0f / 64.0f) + bg0, g1 = acc[ai][0][m][1] * (1.0f / 64.0f) + bg1, u0 = acc[ai][1][m][0] * (1.0f / 64.0f) + bu0, u1 = acc[ai][1][m][1] * (1.0f / 64.0f) + bu1;
;                 const f32x2 h0 = act2((f32x2){g0[0], g0[1]}, (f32x2){u0[0], u0[1]}), h1 = act2((f32x2){g0[2], g0[3]}, (f32x2){u0[2], u0[3]});
;                 const f32x2 h2 = act2((f32x2){g1[0], g1[1]}, (f32x2){u1[0], u1[1]}), h3 = act2((f32x2){g1[2], g1[3]}, (f32x2){u1[2], u1[3]});
;                 *(u32x2*)(Ht + (size_t)rl * FF + hc) = (u32x2){pk4_fp8(h0.x, h0.y, h1.x, h1.y), pk4_fp8(h2.x, h2.y, h3.x, h3.y)}; }
	v_pk_mul_f32 v[26:27], v[34:35], v[26:27]
	v_pk_fma_f32 v[30:31], v[30:31], v[234:235], v[234:235] op_sel:[0,0,1] op_sel_hi:[1,0,1]
	v_pk_mul_f32 v[34:35], v[38:39], v[42:43] op_sel:[1,0] op_sel_hi:[0,0]
	v_pk_mul_f32 v[24:25], v[24:25], v[34:35]
	v_pk_fma_f32 v[32:33], v[116:117], v[242:243], v[228:229] op_sel:[0,1,0] op_sel_hi:[1,1,1] clamp
	v_exp_f32_e32 v34, v30
	v_exp_f32_e32 v35, v31
	v_pk_fma_f32 v[28:29], v[104:105], v[242:243], v[220:221] op_sel_hi:[1,0,1] clamp
	v_pk_fma_f32 v[32:33], v[32:33], v[236:237], v[236:237] op_sel:[0,0,1] op_sel_hi:[1,0,1]
	v_pk_add_f32 v[34:35], v[34:35], 1.0 op_sel_hi:[1,0]
	v_pk_fma_f32 v[40:41], v[110:111], v[242:243], v[214:215] op_sel:[0,1,0] op_sel_hi:[1,1,1] clamp
	v_mul_f32_e32 v38, v34, v35
	v_pk_fma_f32 v[28:29], v[28:29], v[234:235], v[234:235] op_sel:[0,0,1] op_sel_hi:[1,0,1]
	v_pk_mul_f32 v[24:25], v[32:33], v[24:25]
	v_pk_fma_f32 v[32:33], v[40:41], v[236:237], v[236:237] op_sel:[0,0,1] op_sel_hi:[1,0,1]
	v_rcp_f32_e32 v38, v38
	v_pk_fma_f32 v[36:37], v[112:113], v[242:243], v[216:217] op_sel:[0,1,0] op_sel_hi:[1,1,1] clamp
	v_exp_f32_e32 v40, v28
	v_exp_f32_e32 v41, v29
	v_pk_mul_f32 v[34:35], v[34:35], v[38:39] op_sel:[1,0] op_sel_hi:[0,0]
	v_pk_mul_f32 v[30:31], v[30:31], v[34:35]
	v_pk_add_f32 v[34:35], v[40:41], 1.0 op_sel_hi:[1,0]
	v_pk_mul_f32 v[30:31], v[32:33], v[30:31]
	v_mul_f32_e32 v38, v34, v35
	v_rcp_f32_e32 v38, v38
	v_pk_fma_f32 v[32:33], v[36:37], v[236:237], v[236:237] op_sel:[0,0,1] op_sel_hi:[1,0,1]
	v_cvt_pk_fp8_f32 v37, v30, v31
	v_pk_mul_f32 v[34:35], v[34:35], v[38:39] op_sel:[1,0] op_sel_hi:[0,0]
	v_cvt_pk_fp8_f32 v36, v26, v27
	v_pk_mul_f32 v[26:27], v[28:29], v[34:35]
	v_pk_fma_f32 v[34:35], v[98:99], v[242:243], v[226:227] op_sel:[0,1,0] op_sel_hi:[1,1,1] clamp
	v_pk_mul_f32 v[26:27], v[32:33], v[26:27]
	v_cvt_pk_fp8_f32 v36, v24, v25 op_sel:[0,0,1]
	v_cvt_pk_fp8_f32 v37, v26, v27 op_sel:[0,0,1]
	v_pk_fma_f32 v[26:27], v[90:91], v[242:243], v[222:223] op_sel_hi:[1,0,1] clamp
	v_add_co_u32_e32 v24, vcc, s51, v22
	v_pk_fma_f32 v[26:27], v[26:27], v[234:235], v[234:235] op_sel:[0,0,1] op_sel_hi:[1,0,1]
	v_addc_co_u32_e32 v25, vcc, 0, v23, vcc
	v_exp_f32_e32 v38, v26
	v_exp_f32_e32 v39, v27
	global_store_dwordx2 v[24:25], v[36:37], off
	v_pk_fma_f32 v[24:25], v[92:93], v[242:243], v[224:225] op_sel_hi:[1,0,1] clamp
	v_pk_fma_f32 v[34:35], v[34:35], v[236:237], v[236:237] op_sel:[0,0,1] op_sel_hi:[1,0,1]
	v_pk_add_f32 v[38:39], v[38:39], 1.0 op_sel_hi:[1,0]
	v_pk_fma_f32 v[24:25], v[24:25], v[234:235], v[234:235] op_sel:[0,0,1] op_sel_hi:[1,0,1]
	v_mul_f32_e32 v42, v38, v39
	v_rcp_f32_e32 v42, v42
	v_exp_f32_e32 v44, v24
	v_exp_f32_e32 v45, v25
	v_pk_mul_f32 v[38:39], v[38:39], v[42:43] op_sel:[1,0] op_sel_hi:[0,0]
	v_pk_mul_f32 v[26:27], v[26:27], v[38:39]
	v_pk_fma_f32 v[30:31], v[86:87], v[242:243], v[218:219] op_sel_hi:[1,0,1] clamp
	v_pk_add_f32 v[38:39], v[44:45], 1.0 op_sel_hi:[1,0]
	v_mul_f32_e32 v42, v38, v39
	v_rcp_f32_e32 v42, v42
	v_pk_mul_f32 v[26:27], v[34:35], v[26:27]
	v_pk_fma_f32 v[30:31], v[30:31], v[234:235], v[234:235] op_sel:[0,0,1] op_sel_hi:[1,0,1]
	v_pk_mul_f32 v[34:35], v[38:39], v[42:43] op_sel:[1,0] op_sel_hi:[0,0]
	v_pk_mul_f32 v[24:25], v[24:25], v[34:35]
	v_pk_fma_f32 v[32:33], v[100:101], v[242:243], v[228:229] op_sel:[0,1,0] op_sel_hi:[1,1,1] clamp
	v_exp_f32_e32 v34, v30
	v_exp_f32_e32 v35, v31
	v_pk_fma_f32 v[28:29], v[88:89], v[242:243], v[220:221] op_sel_hi:[1,0,1] clamp
	v_pk_fma_f32 v[32:33], v[32:33], v[236:237], v[236:237] op_sel:[0,0,1] op_sel_hi:[1,0,1]
	v_pk_add_f32 v[34:35], v[34:35], 1.0 op_sel_hi:[1,0]
	v_pk_fma_f32 v[40:41], v[94:95], v[242:243], v[214:215] op_sel:[0,1,0] op_sel_hi:[1,1,1] clamp
	v_mul_f32_e32 v38, v34, v35
	v_pk_fma_f32 v[28:29], v[28:29], v[234:235], v[234:235] op_sel:[0,0,1] op_sel_hi:[1,0,1]
	v_pk_mul_f32 v[24:25], v[32:33], v[24:25]
	v_pk_fma_f32 v[32:33], v[40:41], v[236:237], v[236:237] op_sel:[0,0,1] op_sel_hi:[1,0,1]
	v_rcp_f32_e32 v38, v38
	v_pk_fma_f32 v[36:37], v[96:97], v[242:243], v[216:217] op_sel:[0,1,0] op_sel_hi:[1,1,1] clamp
	v_exp_f32_e32 v40, v28
	v_exp_f32_e32 v41, v29
; __device__ __forceinline__ unsigned pk4_fp8(float a, float b, float c, float d) { int w = __builtin_amdgcn_cvt_pk_fp8_f32(a, b, 0, false); w = __builtin_amdgcn_cvt_pk_fp8_f32(c, d, w, true); return (unsigned)w; }
;     static __device__ __forceinline__ f32x2 act2(f32x2 g, f32x2 u) {
;         g.x = __builtin_amdgcn_fmed3f(g.x, -24.0f, 7.0f); g.y = __builtin_amdgcn_fmed3f(g.y, -24.0f, 7.0f);
;         u.x = __builtin_amdgcn_fmed3f(u.x, -7.0f, 7.0f); u.y = __builtin_amdgcn_fmed3f(u.y, -7.0f, 7.0f);
;         f32x2 z = g * (-1.702f * 1.4426950408889634f);
;         f32x2 d; d.x = __builtin_amdgcn_exp2f(z.x); d.y = __builtin_amdgcn_exp2f(z.y);
;         d = d + 1.0f;
;         const float r = __builtin_amdgcn_rcpf(d.x * d.y);
;         f32x2 sg; sg.x = r * d.y; sg.y = r * d.x;
;         return (u + 1.0f) * (g * sg);
;     }
;     __device__ __forceinline__ void operator()(const f32x4 (&acc)[2][2][4][2], const pg8::Unit& u, int wr, int wc, int fr, int fq) const {
;         const int e = u.aux;
;         unsigned char* Ht = ws + WS_H2 + (size_t)u.pm * TSF8;
;         const int hc = u.pn * 128 + wc * 32 + 8 * fq;
;         const f32x4 bg0 = *(const f32x4*)(bgate + e * FF + hc), bg1 = *(const f32x4*)(bgate + e * FF + hc + 4);
;         const f32x4 bu0 = *(const f32x4*)(bup + e * FF + hc), bu1 = *(const f32x4*)(bup + e * FF + hc + 4);
; #pragma unroll
;         for (int ai = 0; ai < 2; ++ai)
; #pragma unroll
;             for (int m = 0; m < 4; ++m) { const int rl = ai * 128 + wr * 64 + m * 16 + fr;
;                 const f32x4 g0 = acc[ai][0][m][0] * (1.0f / 64.0f) + bg0, g1 = acc[ai][0][m][1] * (1.0f / 64.0f) + bg1, u0 = acc[ai][1][m][0] * (1.0f / 64.0f) + bu0, u1 = acc[ai][1][m][1] * (1.0f / 64.0f) + bu1;
;                 const f32x2 h0 = act2((f32x2){g0[0], g0[1]}, (f32x2){u0[0], u0[1]}), h1 = act2((f32x2){g0[2], g0[3]}, (f32x2){u0[2], u0[3]});
;                 const f32x2 h2 = act2((f32x2){g1[0], g1[1]}, (f32x2){u1[0], u1[1]}), h3 = act2((f32x2){g1[2], g1[3]}, (f32x2){u1[2], u1[3]});
;                 *(u32x2*)(Ht + (size_t)rl * FF + hc) = (u32x2){pk4_fp8(h0.x, h0.y, h1.x, h1.y), pk4_fp8(h2.x, h2.y, h3.x, h3.y)}; }
	v_pk_mul_f32 v[34:35], v[34:35], v[38:39] op_sel:[1,0] op_sel_hi:[0,0]
	v_pk_mul_f32 v[30:31], v[30:31], v[34:35]
	v_pk_add_f32 v[34:35], v[40:41], 1.0 op_sel_hi:[1,0]
	v_pk_mul_f32 v[30:31], v[32:33], v[30:31]
	v_mul_f32_e32 v38, v34, v35
	v_rcp_f32_e32 v38, v38
	v_pk_fma_f32 v[32:33], v[36:37], v[236:237], v[236:237] op_sel:[0,0,1] op_sel_hi:[1,0,1]
	v_cvt_pk_fp8_f32 v36, v26, v27
	v_cvt_pk_fp8_f32 v37, v30, v31
	v_pk_mul_f32 v[34:35], v[34:35], v[38:39] op_sel:[1,0] op_sel_hi:[0,0]
	v_pk_mul_f32 v[26:27], v[28:29], v[34:35]
	v_cvt_pk_fp8_f32 v36, v24, v25 op_sel:[0,0,1]
	v_pk_mul_f32 v[26:27], v[32:33], v[26:27]
	v_add_co_u32_e32 v24, vcc, s60, v22
	v_cvt_pk_fp8_f32 v37, v26, v27 op_sel:[0,0,1]
	v_pk_fma_f32 v[14:15], v[74:75], v[242:243], v[222:223] op_sel_hi:[1,0,1] clamp
	v_addc_co_u32_e32 v25, vcc, 0, v23, vcc
	v_pk_fma_f32 v[14:15], v[14:15], v[234:235], v[234:235] op_sel:[0,0,1] op_sel_hi:[1,0,1]
	global_store_dwordx2 v[24:25], v[36:37], off
	v_pk_fma_f32 v[16:17], v[76:77], v[242:243], v[224:225] op_sel_hi:[1,0,1] clamp
	v_exp_f32_e32 v24, v14
	v_exp_f32_e32 v25, v15
	v_pk_fma_f32 v[16:17], v[16:17], v[234:235], v[234:235] op_sel:[0,0,1] op_sel_hi:[1,0,1]
	v_pk_add_f32 v[24:25], v[24:25], 1.0 op_sel_hi:[1,0]
	v_exp_f32_e32 v28, v16
	v_mul_f32_e32 v26, v24, v25
	v_rcp_f32_e32 v26, v26
	v_exp_f32_e32 v29, v17
	v_pk_fma_f32 v[18:19], v[82:83], v[242:243], v[226:227] op_sel:[0,1,0] op_sel_hi:[1,1,1] clamp
	v_pk_fma_f32 v[10:11], v[70:71], v[242:243], v[218:219] op_sel_hi:[1,0,1] clamp
	v_pk_mul_f32 v[24:25], v[24:25], v[26:27] op_sel:[1,0] op_sel_hi:[0,0]
	v_pk_mul_f32 v[14:15], v[14:15], v[24:25]
	v_pk_add_f32 v[24:25], v[28:29], 1.0 op_sel_hi:[1,0]
	v_pk_fma_f32 v[18:19], v[18:19], v[236:237], v[236:237] op_sel:[0,0,1] op_sel_hi:[1,0,1]
	v_mul_f32_e32 v26, v24, v25
	v_rcp_f32_e32 v26, v26
	v_pk_fma_f32 v[20:21], v[84:85], v[242:243], v[228:229] op_sel:[0,1,0] op_sel_hi:[1,1,1] clamp
	v_pk_fma_f32 v[10:11], v[10:11], v[234:235], v[234:235] op_sel:[0,0,1] op_sel_hi:[1,0,1]
	v_pk_mul_f32 v[14:15], v[18:19], v[14:15]
	v_pk_fma_f32 v[18:19], v[20:21], v[236:237], v[236:237] op_sel:[0,0,1] op_sel_hi:[1,0,1]
	v_pk_mul_f32 v[20:21], v[24:25], v[26:27] op_sel:[1,0] op_sel_hi:[0,0]
	v_pk_mul_f32 v[16:17], v[16:17], v[20:21]
	v_exp_f32_e32 v20, v10
	v_exp_f32_e32 v21, v11
	v_pk_fma_f32 v[12:13], v[72:73], v[242:243], v[220:221] op_sel_hi:[1,0,1] clamp
	v_pk_mul_f32 v[16:17], v[18:19], v[16:17]
	v_pk_fma_f32 v[12:13], v[12:13], v[234:235], v[234:235] op_sel:[0,0,1] op_sel_hi:[1,0,1]
	v_pk_add_f32 v[18:19], v[20:21], 1.0 op_sel_hi:[1,0]
	v_mul_f32_e32 v20, v18, v19
	v_rcp_f32_e32 v20, v20
	v_pk_fma_f32 v[6:7], v[78:79], v[242:243], v[214:215] op_sel:[0,1,0] op_sel_hi:[1,1,1] clamp
	v_exp_f32_e32 v24, v12
	v_exp_f32_e32 v25, v13
	v_pk_mul_f32 v[18:19], v[18:19], v[20:21] op_sel:[1,0] op_sel_hi:[0,0]
	v_pk_mul_f32 v[10:11], v[10:11], v[18:19]
	v_pk_fma_f32 v[6:7], v[6:7], v[236:237], v[236:237] op_sel:[0,0,1] op_sel_hi:[1,0,1]
	v_pk_add_f32 v[18:19], v[24:25], 1.0 op_sel_hi:[1,0]
	v_mul_f32_e32 v20, v18, v19
	v_rcp_f32_e32 v20, v20
	v_pk_fma_f32 v[8:9], v[80:81], v[242:243], v[216:217] op_sel:[0,1,0] op_sel_hi:[1,1,1] clamp
	v_pk_mul_f32 v[6:7], v[6:7], v[10:11]
	v_pk_mul_f32 v[10:11], v[18:19], v[20:21] op_sel:[1,0] op_sel_hi:[0,0]
	v_cvt_pk_fp8_f32 v18, v14, v15
	v_cvt_pk_fp8_f32 v19, v6, v7
	v_pk_fma_f32 v[8:9], v[8:9], v[236:237], v[236:237] op_sel:[0,0,1] op_sel_hi:[1,0,1]
	v_pk_mul_f32 v[6:7], v[12:13], v[10:11]
	v_cvt_pk_fp8_f32 v18, v16, v17 op_sel:[0,0,1]
	v_pk_mul_f32 v[6:7], v[8:9], v[6:7]
	s_nop 0
	v_cvt_pk_fp8_f32 v19, v6, v7 op_sel:[0,0,1]
	v_add_co_u32_e32 v6, vcc, 0x2c000, v22
	s_nop 1
	v_addc_co_u32_e32 v7, vcc, 0, v23, vcc
	s_and_b64 vcc, exec, s[2:3]
	s_mov_b64 s[2:3], -1
	global_store_dwordx2 v[6:7], v[18:19], off
	s_cbranch_vccnz .LBB0_956
	s_andn2_b64 vcc, exec, s[10:11]
	s_mov_b64 s[22:23], s[8:9]
	s_mov_b64 s[24:25], s[20:21]
	s_cbranch_vccnz .LBB0_972
	s_lshl_b32 s2, s41, 3
	s_add_i32 s2, s2, s39
	s_ashr_i32 s3, s2, 31
	s_lshl_b64 s[2:3], s[2:3], 18
	s_add_u32 s22, s37, s2
	s_addc_u32 s23, s38, s3
	s_mov_b64 s[24:25], s[6:7]
